# removed 70 compiler over-padding s_nop 0 that followed memory/scalar inline-asm blocks in front of MFMAs in the three mp2 kernels (all MFMA dependency distances re-checked mechanically)
# speedup vs baseline: 1.0066x; 1.0054x over previous
.LBB5_12:
	s_mov_b32 s28, s2
	s_and_b32 s2, s27, 1
	s_waitcnt lgkmcnt(0)
	s_barrier
	s_mul_i32 s33, s2, 0xc000
	v_or_b32_e32 v162, s33, v197
	v_or_b32_e32 v221, s33, v198
	v_or_b32_e32 v230, s33, v199
	s_cmp_eq_u32 s27, 0
	ds_read_b128 v[134:137], v162 offset:0
	ds_read_b128 v[138:141], v162 offset:0x1000
	ds_read_b128 v[158:161], v162 offset:0x2000
	ds_read_b128 v[162:165], v162 offset:0x3000
	ds_read_b128 v[166:169], v221 offset:0
	s_nop 0
	s_waitcnt lgkmcnt(4)
	v_mfma_f32_16x16x32_f16 v[170:173], v[98:101], v[134:137], 0
	ds_read_b128 v[174:177], v221 offset:0x1000
	s_waitcnt lgkmcnt(4)
	v_mfma_f32_16x16x32_f16 v[178:181], v[98:101], v[138:141], 0
	ds_read_b128 v[182:185], v221 offset:0x2000
	s_waitcnt lgkmcnt(4)
	v_mfma_f32_16x16x32_f16 v[186:189], v[98:101], v[158:161], 0
	ds_read_b128 v[222:225], v221 offset:0x3000
	s_waitcnt lgkmcnt(4)
	v_mfma_f32_16x16x32_f16 v[226:229], v[98:101], v[162:165], 0
	ds_read_b128 v[134:137], v230 offset:0
	s_waitcnt lgkmcnt(4)
	v_mfma_f32_16x16x32_f16 v[166:169], v[110:113], v[166:169], v[170:173]
	ds_read_b128 v[138:141], v230 offset:0x1000
	s_waitcnt lgkmcnt(4)
	v_mfma_f32_16x16x32_f16 v[170:173], v[110:113], v[174:177], v[178:181]
	ds_read_b128 v[158:161], v230 offset:0x2000
	s_waitcnt lgkmcnt(4)
	v_mfma_f32_16x16x32_f16 v[174:177], v[110:113], v[182:185], v[186:189]
	ds_read_b128 v[162:165], v230 offset:0x3000
	s_waitcnt lgkmcnt(4)
	v_mfma_f32_16x16x32_f16 v[178:181], v[110:113], v[222:225], v[226:229]
	s_cbranch_scc1 .LBB5_14
	v_exp_f32_e32 v146, v146
	v_exp_f32_e32 v147, v147
	v_exp_f32_e32 v150, v150
	v_exp_f32_e32 v151, v151
	v_add_f32_e32 v146, 1.0, v146
	v_add_f32_e32 v147, 1.0, v147
	v_rcp_f32_e32 v146, v146
	v_rcp_f32_e32 v147, v147
	v_add_f32_e32 v150, 1.0, v150
	v_fmac_f32_e32 v142, v154, v146
	v_fmac_f32_e32 v143, v155, v147
	v_exp_f32_e32 v146, v142
	v_exp_f32_e32 v147, v143
	v_rcp_f32_e32 v142, v150
	v_cvt_f32_f16_e32 v150, v0
	v_add_f32_e32 v143, 1.0, v146
	v_add_f32_e32 v147, 1.0, v147
	v_rcp_f32_e32 v146, v143
	v_add_f32_e32 v143, 1.0, v151
	v_rcp_f32_e32 v147, v147
	v_cvt_f32_f16_sdwa v151, v0 dst_sel:DWORD dst_unused:UNUSED_PAD src0_sel:WORD_1
	v_exp_f32_e32 v0, v148
	v_rcp_f32_e32 v143, v143
	v_pk_fma_f32 v[146:147], v[146:147], 2.0, 1.0 op_sel_hi:[1,0,0] neg_lo:[1,0,0] neg_hi:[1,0,0]
	v_exp_f32_e32 v148, v152
	v_add_f32_e32 v0, 1.0, v0
	v_pk_fma_f32 v[146:147], v[142:143], v[146:147], v[146:147] neg_lo:[1,0,0] neg_hi:[1,0,0]
	v_rcp_f32_e32 v0, v0
	v_pk_fma_f32 v[142:143], v[142:143], v[150:151], v[146:147]
	v_exp_f32_e32 v146, v149
	v_add_f32_e32 v147, 1.0, v148
	v_fmac_f32_e32 v144, v156, v0
	v_exp_f32_e32 v0, v144
	v_add_f32_e32 v144, 1.0, v146
	v_rcp_f32_e32 v146, v144
	v_rcp_f32_e32 v144, v147
	v_exp_f32_e32 v147, v153
	v_add_f32_e32 v0, 1.0, v0
	v_fmac_f32_e32 v145, v157, v146
	v_exp_f32_e32 v148, v145
	v_rcp_f32_e32 v146, v0
	v_add_f32_e32 v0, 1.0, v147
	v_rcp_f32_e32 v145, v0
	v_add_f32_e32 v0, 1.0, v148
	v_rcp_f32_e32 v147, v0
	v_cvt_f32_f16_sdwa v149, v1 dst_sel:DWORD dst_unused:UNUSED_PAD src0_sel:WORD_1
	v_cvt_f32_f16_e32 v148, v1
	v_cvt_pk_f16_f32 v0, v142, v143
	v_pk_fma_f32 v[142:143], v[146:147], 2.0, 1.0 op_sel_hi:[1,0,0] neg_lo:[1,0,0] neg_hi:[1,0,0]
	s_nop 0
	v_pk_fma_f32 v[142:143], v[144:145], v[142:143], v[142:143] neg_lo:[1,0,0] neg_hi:[1,0,0]
	s_nop 0
	v_pk_fma_f32 v[142:143], v[144:145], v[148:149], v[142:143]
	s_nop 0
	v_cvt_pk_f16_f32 v1, v142, v143
	v_add_u32_e32 v142, v206, v217
	global_store_dwordx2 v142, v[0:1], s[0:1] nt
.LBB5_14:
	v_or_b32_e32 v0, s33, v200
	ds_read_b128 v[142:145], v0 offset:0
	s_waitcnt lgkmcnt(4)
	v_mfma_f32_16x16x32_f16 v[134:137], v[114:117], v[134:137], v[166:169]
	ds_read_b128 v[146:149], v0 offset:0x1000
	s_waitcnt lgkmcnt(4)
	v_mfma_f32_16x16x32_f16 v[138:141], v[114:117], v[138:141], v[170:173]
	ds_read_b128 v[150:153], v0 offset:0x2000
	s_waitcnt lgkmcnt(4)
	v_mfma_f32_16x16x32_f16 v[154:157], v[114:117], v[158:161], v[174:177]
	ds_read_b128 v[158:161], v0 offset:0x3000
	s_waitcnt lgkmcnt(4)
	v_mfma_f32_16x16x32_f16 v[162:165], v[114:117], v[162:165], v[178:181]
	ds_read_b128 v[166:169], v205 offset:0
	s_waitcnt lgkmcnt(4)
	v_mfma_f32_16x16x32_f16 v[134:137], v[106:109], v[142:145], v[134:137]
	ds_read_b128 v[142:145], v205 offset:0x100
	s_waitcnt lgkmcnt(4)
	v_mfma_f32_16x16x32_f16 v[138:141], v[106:109], v[146:149], v[138:141]
	ds_read_b128 v[146:149], v205 offset:0x200
	s_waitcnt lgkmcnt(4)
	v_mfma_f32_16x16x32_f16 v[150:153], v[106:109], v[150:153], v[154:157]
	ds_read_b128 v[154:157], v205 offset:0x300
	s_waitcnt lgkmcnt(4)
	v_mfma_f32_16x16x32_f16 v[158:161], v[106:109], v[158:161], v[162:165]
	s_waitcnt lgkmcnt(3)
	v_mfma_f32_16x16x32_f16 v[134:137], v[102:105], v[166:169], v[134:137]
	s_waitcnt lgkmcnt(2)
	v_mfma_f32_16x16x32_f16 v[138:141], v[102:105], v[142:145], v[138:141]
	s_waitcnt lgkmcnt(1)
	v_mfma_f32_16x16x32_f16 v[142:145], v[102:105], v[146:149], v[150:153]
	s_waitcnt lgkmcnt(0)
	v_mfma_f32_16x16x32_f16 v[146:149], v[102:105], v[154:157], v[158:161]
	s_nop 1
	v_cvt_pk_f16_f32 v1, v136, v137
	v_pk_max_f16 v1, v1, 0
	v_cvt_pk_f16_f32 v0, v134, v135
	v_pk_max_f16 v0, v0, 0
	v_cvt_pk_f16_f32 v135, v140, v141
	v_pk_max_f16 v135, v135, 0
	v_cvt_pk_f16_f32 v134, v138, v139
	v_pk_max_f16 v134, v134, 0
	ds_write2st64_b64 v218, v[0:1], v[134:135] offset1:8
	v_cvt_pk_f16_f32 v1, v144, v145
	v_pk_max_f16 v1, v1, 0
	v_cvt_pk_f16_f32 v0, v142, v143
	v_pk_max_f16 v0, v0, 0
	s_lshl_b32 s34, s2, 14
	v_cvt_pk_f16_f32 v135, v148, v149
	v_pk_max_f16 v135, v135, 0
	v_cvt_pk_f16_f32 v134, v146, v147
	v_pk_max_f16 v134, v134, 0
	s_or_b32 s34, s34, 0x18000
	ds_write2st64_b64 v218, v[0:1], v[134:135] offset0:16 offset1:24
	v_or_b32_e32 v172, s34, v197
	v_or_b32_e32 v223, s34, v198
	v_or_b32_e32 v143, s34, v199
	v_or_b32_e32 v142, s34, v200
	v_add_u32_e32 v0, s34, v208
	s_xor_b32 s34, s2, 1
	s_waitcnt vmcnt(2) lgkmcnt(0)
	s_barrier
	ds_read_b128 v[134:137], v201 offset:0
	s_mul_i32 s37, s34, 0xc000
	ds_read_b128 v[138:141], v202 offset:0
	ds_read_b128 v[144:147], v203 offset:0
	ds_read_b128 v[148:151], v204 offset:0
	v_add_u32_e32 v1, s37, v209
	ds_read_b128 v[152:155], v1 offset:0
	ds_read_b128 v[156:159], v1 offset:0x4000
	ds_read_b128 v[160:163], v1 offset:0x8000
	ds_read_b128 v[164:167], v1 offset:0x400
	ds_read_b128 v[168:171], v1 offset:0x4400
	ds_read_b128 v[174:177], v1 offset:0x8400
	ds_read_b128 v[178:181], v172 offset:0
	s_waitcnt lgkmcnt(10)
	v_subrev_u32_e32 v186, 56, v215
	v_mfma_f32_16x16x32_f16 v[182:185], v[2:5], v[134:137], v[118:121]
	v_min_u32_e32 v225, s17, v186
	v_mfma_f32_16x16x32_f16 v[186:189], v[42:45], v[134:137], v[122:125]
	ds_read_b128 v[226:229], v223 offset:0
	s_waitcnt lgkmcnt(10)
	v_mfma_f32_16x16x32_f16 v[134:137], v[66:69], v[134:137], v[126:129]
	v_lshl_or_b32 v173, v196, 8, v190
	v_mfma_f32_16x16x32_f16 v[182:185], v[6:9], v[138:141], v[182:185]
	v_add_u32_e32 v196, -8, v215
	v_min_u32_e32 v238, s17, v196
	v_subrev_u32_e32 v196, 52, v215
	v_mfma_f32_16x16x32_f16 v[186:189], v[46:49], v[138:141], v[186:189]
	v_add_u32_e32 v221, -4, v215
	v_min_u32_e32 v196, s18, v196
	v_min_u32_e32 v221, s18, v221
	v_mfma_f32_16x16x32_f16 v[230:233], v[70:73], v[138:141], v[134:137]
	s_cmp_lg_u32 s42, 0
	s_cbranch_scc1 .Lmp0_nofeat
	v_add_u32_e32 v224, s20, v216
	v_cmp_gt_u32_e32 vcc, s8, v224
	v_mov_b32_e32 v234, s16
	s_nop 0
	v_cndmask_b32_e32 v234, v234, v224, vcc
	v_lshlrev_b32_e32 v234, 5, v234
	global_load_dwordx4 v[134:137], v234, s[6:7]
	global_load_dwordx4 v[138:141], v234, s[6:7] offset:16
.Lmp0_nofeat:
	ds_read_b128 v[234:237], v143 offset:0
	s_waitcnt lgkmcnt(10)
	v_lshl_or_b32 v242, v192, 8, v190
	v_mfma_f32_16x16x32_f16 v[182:185], v[50:53], v[144:147], v[182:185]
	global_load_dword v192, v196, s[4:5]
	v_subrev_u32_e32 v239, 48, v215
	global_load_dword v221, v221, s[4:5]
	v_mfma_f32_16x16x32_f16 v[186:189], v[18:21], v[144:147], v[186:189]
	v_min_u32_e32 v222, s19, v215
	v_min_u32_e32 v239, s19, v239
	v_lshl_or_b32 v241, v194, 8, v191
	v_mfma_f32_16x16x32_f16 v[144:147], v[74:77], v[144:147], v[230:233]
	global_load_dword v196, v239, s[4:5]
	ds_read_b128 v[230:233], v142 offset:0
	s_waitcnt lgkmcnt(10)
	global_load_dword v194, v222, s[4:5]
	s_add_i32 s2, s28, s3
	v_mfma_f32_16x16x32_f16 v[182:185], v[10:13], v[148:151], v[182:185]
	v_lshl_or_b32 v243, v193, 8, v190
	global_load_dword v193, v225, s[4:5]
	s_min_i32 s35, s2, s14
	v_mfma_f32_16x16x32_f16 v[186:189], v[58:61], v[148:151], v[186:189]
	global_load_dword v222, v238, s[4:5]
	s_lshl_b32 s35, s35, 14
	s_lshl_b32 s34, s34, 14
	v_mfma_f32_16x16x32_f16 v[148:151], v[90:93], v[148:151], v[144:147]
	s_add_i32 s36, s33, 0
	v_add_u32_e32 v1, s35, v210
	s_add_i32 s38, s25, s34
	s_add_i32 s39, s36, s21
	s_add_i32 s40, s26, s34
	s_add_i32 s34, s36, s23
	s_add_i32 m0, s39, 0x8000
	v_add_u32_e32 v240, s35, v211
	s_add_i32 s41, s34, 0x8000
	s_add_i32 s35, s39, 0x4000
	s_add_i32 s36, s22, s33
	v_add_u32_e32 v239, s37, v212
	ds_read_b128 v[144:147], v201 offset:0x1000
	s_waitcnt lgkmcnt(4)
	s_waitcnt lgkmcnt(5)
	s_nop 0
	v_pk_add_f16 v152, v152, v156
	v_pk_add_f16 v153, v153, v157
	v_pk_add_f16 v154, v154, v158
	v_pk_add_f16 v155, v155, v159
	v_pk_add_f16 v154, v154, v162
	v_pk_add_f16 v155, v155, v163
	v_pk_add_f16 v153, v153, v161
	v_pk_add_f16 v152, v152, v160
	ds_write_b128 v239, v[152:155]
	v_pk_add_f16 v152, v164, v168
	v_pk_add_f16 v153, v165, v169
	v_pk_add_f16 v154, v166, v170
	v_pk_add_f16 v155, v167, v171
	v_pk_add_f16 v154, v154, v176
	v_pk_add_f16 v155, v155, v177
	v_pk_add_f16 v153, v153, v175
	v_pk_add_f16 v152, v152, v174
	ds_write_b128 v239, v[152:155] offset:1024
	ds_read_b128 v[152:155], v202 offset:0x1000
	s_waitcnt lgkmcnt(4)
	global_load_lds_dwordx4 v173, s[12:13]
	s_mov_b32 m0, s38
	ds_read_b128 v[168:171], v203 offset:0x1000
	s_waitcnt lgkmcnt(4)
	v_mfma_f32_16x16x32_f16 v[182:185], v[14:17], v[178:181], v[182:185]
	global_load_lds_dwordx4 v1, s[12:13]
	ds_read_b128 v[174:177], v204 offset:0x1000
	v_mfma_f32_16x16x32_f16 v[186:189], v[22:25], v[178:181], v[186:189]
	s_waitcnt lgkmcnt(4)
	v_mfma_f32_16x16x32_f16 v[178:181], v[86:89], v[178:181], v[130:133]
	v_mfma_f32_16x16x32_f16 v[156:159], v[26:29], v[226:229], v[182:185]
	v_mfma_f32_16x16x32_f16 v[160:163], v[34:37], v[226:229], v[186:189]
	v_mfma_f32_16x16x32_f16 v[164:167], v[78:81], v[226:229], v[178:181]
	v_mfma_f32_16x16x32_f16 v[156:159], v[30:33], v[234:237], v[156:159]
	v_mfma_f32_16x16x32_f16 v[160:163], v[38:41], v[234:237], v[160:163]
	v_mfma_f32_16x16x32_f16 v[164:167], v[82:85], v[234:237], v[164:167]
	v_mfma_f32_16x16x32_f16 v[156:159], v[54:57], v[230:233], v[156:159]
	v_mfma_f32_16x16x32_f16 v[160:163], v[62:65], v[230:233], v[160:163]
	v_mfma_f32_16x16x32_f16 v[164:167], v[94:97], v[230:233], v[164:167]
	s_mov_b32 m0, s41
	ds_read_b64 v[234:235], v0 offset:0
	ds_read_b128 v[178:181], v172 offset:0x1000
	s_waitcnt lgkmcnt(5)
	ds_read_b128 v[186:189], v223 offset:0x1000
	s_waitcnt lgkmcnt(5)
	s_nop 4
	v_exp_f32_e32 v1, v156
	s_waitcnt lgkmcnt(2)
	ds_read_b128 v[230:233], v143 offset:0x1000
	s_waitcnt lgkmcnt(5)
	global_load_lds_dwordx4 v241, s[12:13]
	v_add_f32_e32 v1, 1.0, v1
	v_rcp_f32_e32 v1, v1
	v_exp_f32_e32 v156, v160
	v_mfma_f32_16x16x32_f16 v[182:185], v[2:5], v[144:147], v[118:121]
	v_add_u32_e32 v225, v206, v213
	v_fma_f32 v1, v1, v164, v148
	v_exp_f32_e32 v1, v1
	v_add_f32_e32 v148, 1.0, v156
	v_exp_f32_e32 v156, v157
	v_rcp_f32_e32 v148, v148
	v_add_f32_e32 v1, 1.0, v1
	v_rcp_f32_e32 v1, v1
	v_add_f32_e32 v156, 1.0, v156
	v_rcp_f32_e32 v156, v156
	v_mfma_f32_16x16x32_f16 v[226:229], v[42:45], v[144:147], v[122:125]
	v_fma_f32 v1, v1, -2.0, 1.0
	v_fma_f32 v1, -v148, v1, v1
	v_fma_mixlo_f16 v1, v148, v234, v1 op_sel_hi:[0,1,0]
	v_mfma_f32_16x16x32_f16 v[144:147], v[66:69], v[144:147], v[126:129]
	v_exp_f32_e32 v148, v161
	v_fma_f32 v149, v156, v165, v149
	v_exp_f32_e32 v149, v149
	v_mfma_f32_16x16x32_f16 v[182:185], v[6:9], v[152:155], v[182:185]
	v_add_f32_e32 v148, 1.0, v148
	v_rcp_f32_e32 v156, v148
	v_add_f32_e32 v148, 1.0, v149
	v_mfma_f32_16x16x32_f16 v[226:229], v[46:49], v[152:155], v[226:229]
	v_rcp_f32_e32 v157, v148
	v_add_u32_e32 v173, 0x1000, v225
	v_mfma_f32_16x16x32_f16 v[144:147], v[70:73], v[152:155], v[144:147]
	v_mfma_f32_16x16x32_f16 v[152:155], v[50:53], v[168:171], v[182:185]
	v_mfma_f32_16x16x32_f16 v[182:185], v[18:21], v[168:171], v[226:229]
	v_mfma_f32_16x16x32_f16 v[144:147], v[74:77], v[168:171], v[144:147]
	ds_read_b128 v[168:171], v142 offset:0x1000
	s_waitcnt lgkmcnt(5)
	v_mfma_f32_16x16x32_f16 v[152:155], v[10:13], v[174:177], v[152:155]
	v_mfma_f32_16x16x32_f16 v[182:185], v[58:61], v[174:177], v[182:185]
	v_mfma_f32_16x16x32_f16 v[146:149], v[90:93], v[174:177], v[144:147]
	s_nop 3
	v_fma_f32 v144, v157, -2.0, 1.0
	v_fma_f32 v144, -v156, v144, v144
	v_fma_mixlo_f16 v144, v156, v234, v144 op_sel:[0,1,0] op_sel_hi:[0,1,0]
	s_mov_b32 m0, s40
	ds_read_b128 v[174:177], v201 offset:0x2000
	s_waitcnt lgkmcnt(4)
	ds_read_b128 v[226:229], v202 offset:0x2000
	s_waitcnt lgkmcnt(4)
	v_exp_f32_e32 v145, v158
	global_load_lds_dwordx4 v240, s[12:13]
	v_exp_f32_e32 v156, v162
	v_add_f32_e32 v145, 1.0, v145
	v_rcp_f32_e32 v145, v145
	v_mfma_f32_16x16x32_f16 v[152:155], v[14:17], v[178:181], v[152:155]
	v_pack_b32_f16 v144, v1, v144
	v_fma_f32 v145, v145, v166, v150
	v_add_f32_e32 v150, 1.0, v156
	v_rcp_f32_e32 v234, v150
	v_exp_f32_e32 v150, v159
	v_mfma_f32_16x16x32_f16 v[182:185], v[22:25], v[178:181], v[182:185]
	v_exp_f32_e32 v145, v145
	v_add_f32_e32 v150, 1.0, v150
	v_mfma_f32_16x16x32_f16 v[178:181], v[86:89], v[178:181], v[130:133]
	v_rcp_f32_e32 v150, v150
	v_add_f32_e32 v145, 1.0, v145
	v_rcp_f32_e32 v145, v145
	v_mfma_f32_16x16x32_f16 v[182:185], v[34:37], v[186:189], v[182:185]
	v_fmac_f32_e32 v151, v150, v167
	v_fma_f32 v145, v145, -2.0, 1.0
	v_mfma_f32_16x16x32_f16 v[178:181], v[78:81], v[186:189], v[178:181]
	v_fma_f32 v145, -v234, v145, v145
	v_fma_mixlo_f16 v145, v234, v235, v145 op_sel_hi:[0,1,0]
	v_mfma_f32_16x16x32_f16 v[152:155], v[26:29], v[186:189], v[152:155]
	ds_read_b128 v[186:189], v203 offset:0x2000
	s_waitcnt lgkmcnt(4)
	ds_read_b128 v[164:167], v204 offset:0x2000
	s_waitcnt lgkmcnt(4)
	v_mfma_f32_16x16x32_f16 v[156:159], v[38:41], v[230:233], v[182:185]
	s_nop 2
	v_exp_f32_e32 v182, v163
	v_mfma_f32_16x16x32_f16 v[160:163], v[82:85], v[230:233], v[178:181]
	s_nop 2
	v_exp_f32_e32 v178, v151
	v_mfma_f32_16x16x32_f16 v[152:155], v[30:33], v[230:233], v[152:155]
	v_add_f32_e32 v179, 1.0, v182
	v_add_f32_e32 v178, 1.0, v178
	v_mfma_f32_16x16x32_f16 v[150:153], v[54:57], v[168:171], v[152:155]
	v_mfma_f32_16x16x32_f16 v[154:157], v[62:65], v[168:171], v[156:159]
	s_nop 2
	v_rcp_f32_e32 v158, v178
	v_rcp_f32_e32 v159, v179
	v_mfma_f32_16x16x32_f16 v[168:171], v[94:97], v[168:171], v[160:163]
	v_fma_f32 v158, v158, -2.0, 1.0
	v_fma_f32 v158, -v159, v158, v158
	v_fma_mixlo_f16 v158, v159, v235, v158 op_sel:[0,1,0] op_sel_hi:[0,1,0]
	s_nop 0
	v_pack_b32_f16 v145, v145, v158
	global_store_dwordx2 v173, v[144:145], s[0:1] nt
	s_mov_b32 m0, s36
	ds_read_b64 v[238:239], v0 offset:0x1000
	ds_read_b128 v[178:181], v172 offset:0x2000
	s_waitcnt lgkmcnt(5)
	ds_read_b128 v[182:185], v223 offset:0x2000
	s_waitcnt lgkmcnt(5)
	v_exp_f32_e32 v1, v150
	s_waitcnt lgkmcnt(2)
	ds_read_b128 v[234:237], v143 offset:0x2000
	s_waitcnt lgkmcnt(5)
	global_load_lds_dwordx4 v243, s[12:13]
	v_add_f32_e32 v1, 1.0, v1
	v_rcp_f32_e32 v1, v1
	v_exp_f32_e32 v145, v151
	v_mfma_f32_16x16x32_f16 v[158:161], v[2:5], v[174:177], v[118:121]
	v_exp_f32_e32 v144, v154
	v_fma_f32 v1, v1, v168, v146
	v_exp_f32_e32 v1, v1
	v_mfma_f32_16x16x32_f16 v[230:233], v[42:45], v[174:177], v[122:125]
	v_add_f32_e32 v145, 1.0, v145
	v_rcp_f32_e32 v145, v145
	v_add_f32_e32 v1, 1.0, v1
	v_mfma_f32_16x16x32_f16 v[174:177], v[66:69], v[174:177], v[126:129]
	v_add_f32_e32 v144, 1.0, v144
	v_rcp_f32_e32 v1, v1
	v_rcp_f32_e32 v144, v144
	v_mfma_f32_16x16x32_f16 v[158:161], v[6:9], v[226:229], v[158:161]
	v_fma_f32 v145, v145, v169, v147
	v_exp_f32_e32 v145, v145
	v_exp_f32_e32 v146, v155
	v_mfma_f32_16x16x32_f16 v[174:177], v[70:73], v[226:229], v[174:177]
	v_fma_f32 v1, v1, -2.0, 1.0
	v_fma_f32 v1, -v144, v1, v1
	v_fma_mixlo_f16 v240, v144, v238, v1 op_sel_hi:[0,1,0]
	v_mfma_f32_16x16x32_f16 v[230:233], v[46:49], v[226:229], v[230:233]
	v_add_f32_e32 v144, 1.0, v145
	v_add_f32_e32 v1, 1.0, v146
	v_rcp_f32_e32 v150, v144
	v_mfma_f32_16x16x32_f16 v[158:161], v[50:53], v[186:189], v[158:161]
	v_rcp_f32_e32 v1, v1
	v_add_u32_e32 v173, 0x2000, v225
	v_fma_f32 v150, v150, -2.0, 1.0
	v_mfma_f32_16x16x32_f16 v[174:177], v[74:77], v[186:189], v[174:177]
	v_fma_f32 v243, -v1, v150, v150
	v_mfma_f32_16x16x32_f16 v[226:229], v[18:21], v[186:189], v[230:233]
	ds_read_b128 v[186:189], v142 offset:0x2000
	s_waitcnt lgkmcnt(5)
	v_mfma_f32_16x16x32_f16 v[158:161], v[10:13], v[164:167], v[158:161]
	v_mfma_f32_16x16x32_f16 v[144:147], v[90:93], v[164:167], v[174:177]
	v_mfma_f32_16x16x32_f16 v[226:229], v[58:61], v[164:167], v[226:229]
	s_mov_b32 m0, s35
	ds_read_b128 v[230:233], v201 offset:0x3000
	s_waitcnt lgkmcnt(4)
	v_exp_f32_e32 v150, v152
	v_mfma_f32_16x16x32_f16 v[164:167], v[14:17], v[178:181], v[158:161]
	ds_read_b128 v[160:163], v202 offset:0x3000
	s_waitcnt lgkmcnt(4)
	global_load_lds_dwordx4 v242, s[12:13]
	v_exp_f32_e32 v154, v153
	v_add_f32_e32 v150, 1.0, v150
	v_rcp_f32_e32 v150, v150
	v_mfma_f32_16x16x32_f16 v[174:177], v[22:25], v[178:181], v[226:229]
	v_add_f32_e32 v154, 1.0, v154
	v_rcp_f32_e32 v154, v154
	v_exp_f32_e32 v151, v156
	v_mfma_f32_16x16x32_f16 v[178:181], v[86:89], v[178:181], v[130:133]
	v_fma_f32 v148, v150, v170, v148
	v_exp_f32_e32 v148, v148
	v_fmac_f32_e32 v149, v154, v171
	v_mfma_f32_16x16x32_f16 v[226:229], v[26:29], v[182:185], v[164:167]
	v_exp_f32_e32 v149, v149
	v_add_f32_e32 v150, 1.0, v151
	v_rcp_f32_e32 v241, v150
	v_mfma_f32_16x16x32_f16 v[174:177], v[34:37], v[182:185], v[174:177]
	v_add_f32_e32 v148, 1.0, v148
	ds_read_b128 v[164:167], v203 offset:0x3000
	s_waitcnt lgkmcnt(4)
	v_mfma_f32_16x16x32_f16 v[178:181], v[78:81], v[182:185], v[178:181]
	v_exp_f32_e32 v155, v157
	v_rcp_f32_e32 v148, v148
	v_add_f32_e32 v149, 1.0, v149
	v_mfma_f32_16x16x32_f16 v[150:153], v[30:33], v[234:237], v[226:229]
	v_rcp_f32_e32 v149, v149
	ds_read_b128 v[168:171], v204 offset:0x3000
	s_waitcnt lgkmcnt(4)
	v_mfma_f32_16x16x32_f16 v[174:177], v[38:41], v[234:237], v[174:177]
	v_fma_f32 v148, v148, -2.0, 1.0
	v_fma_f32 v148, -v241, v148, v148
	v_fma_mixlo_f16 v241, v241, v239, v148 op_sel_hi:[0,1,0]
	v_mfma_f32_16x16x32_f16 v[178:181], v[82:85], v[234:237], v[178:181]
	v_fma_mixhi_f16 v240, v1, v238, v243 op_sel:[0,1,0] op_sel_hi:[0,1,0]
	v_mfma_f32_16x16x32_f16 v[156:159], v[54:57], v[186:189], v[150:153]
	s_nop 2
	v_add_f32_e32 v150, 1.0, v155
	v_mfma_f32_16x16x32_f16 v[152:155], v[62:65], v[186:189], v[174:177]
	s_nop 2
	v_rcp_f32_e32 v174, v150
	v_fma_f32 v175, v149, -2.0, 1.0
	v_mfma_f32_16x16x32_f16 v[148:151], v[94:97], v[186:189], v[178:181]
	v_fma_f32 v175, -v174, v175, v175
	v_fma_mixhi_f16 v241, v174, v239, v175 op_sel:[0,1,0] op_sel_hi:[0,1,0]
	global_store_dwordx2 v173, v[240:241], s[0:1] nt
	ds_read_b64 v[188:189], v0 offset:0x2000
	ds_read_b64 v[0:1], v0 offset:0x3000
	ds_read_b128 v[172:175], v172 offset:0x3000
	s_waitcnt lgkmcnt(6)
	s_andn2_b64 vcc, exec, s[10:11]
	v_mfma_f32_16x16x32_f16 v[180:183], v[2:5], v[230:233], v[118:121]
	s_waitcnt vmcnt(14)
	v_mfma_f32_16x16x32_f16 v[176:179], v[42:45], v[230:233], v[122:125]
	v_mfma_f32_16x16x32_f16 v[184:187], v[66:69], v[230:233], v[126:129]
	s_cbranch_vccnz .LBB5_11
	v_cvt_pk_f16_f32 v226, v134, v135
	v_cvt_pk_f16_f32 v227, v136, v137
	v_cvt_pk_f16_f32 v228, v138, v139
	v_cvt_pk_f16_f32 v229, v140, v141
	s_add_i32 s46, s20, s30
	s_add_i32 s46, s46, 63
	s_cmp_lt_i32 s46, s8
	s_cbranch_scc1 .Lmp0_fb_nomask
	v_cmp_gt_i32_e32 vcc, s8, v224
	s_nop 1
	v_cndmask_b32_e32 v226, 0, v226, vcc
	v_cndmask_b32_e32 v227, 0, v227, vcc
	v_cndmask_b32_e32 v228, 0, v228, vcc
	v_cndmask_b32_e32 v229, 0, v229, vcc

.LBB6_14:
	s_and_b32 s23, s19, 0x1000
	v_or_b32_e32 v150, s23, v202
	v_cndmask_b32_e64 v150, v217, v150, s[4:5]
	s_waitcnt lgkmcnt(0)
	s_barrier
	v_add_u32_e32 v166, 0, v150
	ds_read_b128 v[150:153], v166
	ds_read_b128 v[154:157], v166 offset:1024
	ds_read_b128 v[158:161], v166 offset:3072
	ds_read_b128 v[162:165], v166 offset:2048
	s_waitcnt lgkmcnt(0)
	v_mfma_f32_16x16x32_f16 v[150:153], v[102:105], v[150:153], 0
	v_add_u32_e32 v167, 0, v203
	v_add_u32_e32 v168, 0x18000, v167
	s_mov_b32 s22, s2
	v_mfma_f32_16x16x32_f16 v[154:157], v[102:105], v[154:157], 0
	s_nop 3
	v_max_i32_e32 v151, 0, v151
	v_max_i32_e32 v150, 0, v150
	v_max_i32_e32 v153, 0, v153
	v_mfma_f32_16x16x32_f16 v[162:165], v[102:105], v[162:165], 0
	v_max_i32_e32 v152, 0, v152
	v_max_i32_e32 v155, 0, v155
	v_max_i32_e32 v154, 0, v154
	v_mfma_f32_16x16x32_f16 v[158:161], v[102:105], v[158:161], 0
	v_add_f32_e64 v150, v150, v154
	v_add_f32_e64 v151, v151, v155
	s_nop 1
	v_max_i32_e32 v155, 0, v163
	v_max_i32_e32 v154, 0, v162
	v_pk_add_f32 v[150:151], v[150:151], v[154:155]
	v_max_i32_e32 v155, 0, v157
	v_max_i32_e32 v154, 0, v156
	v_pk_add_f32 v[152:153], v[152:153], v[154:155]
	v_max_i32_e32 v155, 0, v165
	v_max_i32_e32 v154, 0, v164
	v_pk_add_f32 v[152:153], v[152:153], v[154:155]
	v_cvt_pk_f16_f32 v150, v150, v151
	v_cvt_pk_f16_f32 v151, v152, v153
	v_cvt_pk_f16_f32 v153, v160, v161
	v_pk_max_f16 v153, v153, 0
	v_cvt_pk_f16_f32 v152, v158, v159
	v_pk_max_f16 v152, v152, 0
	ds_write_b64 v167, v[150:151]
	ds_write_b64 v168, v[152:153]
	ds_read_b128 v[150:153], v166 offset:256
	ds_read_b128 v[154:157], v166 offset:1280
	ds_read_b128 v[158:161], v166 offset:2304
	ds_read_b128 v[162:165], v166 offset:3328
	s_waitcnt lgkmcnt(3)
	v_mfma_f32_16x16x32_f16 v[150:153], v[102:105], v[150:153], 0
	v_subrev_co_u32_e32 v215, vcc, 1, v215
	s_waitcnt lgkmcnt(2)
	v_mfma_f32_16x16x32_f16 v[154:157], v[102:105], v[154:157], 0
	s_nop 4
	v_max_i32_e32 v151, 0, v151
	v_max_i32_e32 v150, 0, v150
	v_max_i32_e32 v153, 0, v153
	s_waitcnt lgkmcnt(1)
	v_mfma_f32_16x16x32_f16 v[158:161], v[102:105], v[158:161], 0
	v_max_i32_e32 v152, 0, v152
	v_max_i32_e32 v155, 0, v155
	v_max_i32_e32 v154, 0, v154
	s_waitcnt lgkmcnt(0)
	v_mfma_f32_16x16x32_f16 v[162:165], v[102:105], v[162:165], 0
	v_add_f32_e64 v150, v150, v154
	v_add_f32_e64 v151, v151, v155
	s_nop 0
	v_max_i32_e32 v155, 0, v159
	v_max_i32_e32 v154, 0, v158
	v_pk_add_f32 v[150:151], v[150:151], v[154:155]
	v_max_i32_e32 v155, 0, v157
	v_max_i32_e32 v154, 0, v156
	v_pk_add_f32 v[152:153], v[152:153], v[154:155]
	v_max_i32_e32 v155, 0, v161
	v_max_i32_e32 v154, 0, v160
	v_pk_add_f32 v[152:153], v[152:153], v[154:155]
	v_cvt_pk_f16_f32 v150, v150, v151
	v_cvt_pk_f16_f32 v151, v152, v153
	v_cvt_pk_f16_f32 v153, v164, v165
	v_pk_max_f16 v153, v153, 0
	v_cvt_pk_f16_f32 v152, v162, v163
	v_pk_max_f16 v152, v152, 0
	ds_write_b64 v167, v[150:151] offset:4096
	ds_write_b64 v168, v[152:153] offset:4096
	ds_read_b128 v[150:153], v166 offset:512
	ds_read_b128 v[154:157], v166 offset:1536
	ds_read_b128 v[158:161], v166 offset:2560
	ds_read_b128 v[162:165], v166 offset:3584
	s_waitcnt lgkmcnt(3)
	v_mfma_f32_16x16x32_f16 v[150:153], v[102:105], v[150:153], 0
	s_waitcnt lgkmcnt(2)
	v_mfma_f32_16x16x32_f16 v[154:157], v[102:105], v[154:157], 0
	s_nop 5
	v_max_i32_e32 v151, 0, v151
	v_max_i32_e32 v150, 0, v150
	v_max_i32_e32 v153, 0, v153
	s_waitcnt lgkmcnt(1)
	v_mfma_f32_16x16x32_f16 v[158:161], v[102:105], v[158:161], 0
	v_max_i32_e32 v152, 0, v152
	v_max_i32_e32 v155, 0, v155
	v_max_i32_e32 v154, 0, v154
	s_waitcnt lgkmcnt(0)
	v_mfma_f32_16x16x32_f16 v[162:165], v[102:105], v[162:165], 0
	v_add_f32_e64 v150, v150, v154
	v_add_f32_e64 v151, v151, v155
	s_nop 0
	v_max_i32_e32 v155, 0, v159
	v_max_i32_e32 v154, 0, v158
	v_pk_add_f32 v[150:151], v[150:151], v[154:155]
	v_max_i32_e32 v155, 0, v157
	v_max_i32_e32 v154, 0, v156
	v_pk_add_f32 v[152:153], v[152:153], v[154:155]
	v_max_i32_e32 v155, 0, v161
	v_max_i32_e32 v154, 0, v160
	v_pk_add_f32 v[152:153], v[152:153], v[154:155]
	v_cvt_pk_f16_f32 v150, v150, v151
	v_cvt_pk_f16_f32 v151, v152, v153
	v_cvt_pk_f16_f32 v153, v164, v165
	v_pk_max_f16 v153, v153, 0
	v_cvt_pk_f16_f32 v152, v162, v163
	v_pk_max_f16 v152, v152, 0
	ds_write_b64 v167, v[150:151] offset:8192
	ds_write_b64 v168, v[152:153] offset:8192
	ds_read_b128 v[150:153], v166 offset:768
	ds_read_b128 v[154:157], v166 offset:1792
	ds_read_b128 v[158:161], v166 offset:2816
	ds_read_b128 v[162:165], v166 offset:3840
	s_waitcnt lgkmcnt(3)
	v_mfma_f32_16x16x32_f16 v[150:153], v[102:105], v[150:153], 0
	s_waitcnt lgkmcnt(2)
	v_mfma_f32_16x16x32_f16 v[154:157], v[102:105], v[154:157], 0
	s_nop 5
	v_max_i32_e32 v151, 0, v151
	v_max_i32_e32 v150, 0, v150
	v_max_i32_e32 v153, 0, v153
	s_waitcnt lgkmcnt(1)
	v_mfma_f32_16x16x32_f16 v[158:161], v[102:105], v[158:161], 0
	v_max_i32_e32 v152, 0, v152
	v_max_i32_e32 v155, 0, v155
	v_max_i32_e32 v154, 0, v154
	s_waitcnt lgkmcnt(0)
	v_mfma_f32_16x16x32_f16 v[162:165], v[102:105], v[162:165], 0
	v_add_f32_e64 v150, v150, v154
	v_add_f32_e64 v151, v151, v155
	s_nop 0
	v_max_i32_e32 v155, 0, v159
	v_max_i32_e32 v154, 0, v158
	v_pk_add_f32 v[150:151], v[150:151], v[154:155]
	v_max_i32_e32 v155, 0, v157
	v_max_i32_e32 v154, 0, v156
	v_pk_add_f32 v[152:153], v[152:153], v[154:155]
	v_max_i32_e32 v155, 0, v161
	v_max_i32_e32 v154, 0, v160
	v_pk_add_f32 v[152:153], v[152:153], v[154:155]
	v_cvt_pk_f16_f32 v150, v150, v151
	v_cvt_pk_f16_f32 v151, v152, v153
	v_cvt_pk_f16_f32 v153, v164, v165
	v_pk_max_f16 v153, v153, 0
	v_cvt_pk_f16_f32 v152, v162, v163
	v_pk_max_f16 v152, v152, 0
	ds_write_b64 v167, v[150:151] offset:12288
	ds_write_b64 v168, v[152:153] offset:12288
	s_waitcnt lgkmcnt(0)
	s_barrier
	ds_read_b128 v[150:153], v192 offset:0
	ds_read_b128 v[154:157], v192 offset:0x1000
	ds_read_b128 v[158:161], v192 offset:0x2000
	ds_read_b128 v[162:165], v192 offset:0x3000
	ds_read_b128 v[166:169], v194 offset:0
	s_nop 0
	s_waitcnt lgkmcnt(4)
	v_mfma_f32_16x16x32_f16 v[170:173], v[98:101], v[150:153], 0
	ds_read_b128 v[174:177], v194 offset:0x1000
	s_waitcnt lgkmcnt(4)
	v_mfma_f32_16x16x32_f16 v[178:181], v[98:101], v[154:157], 0
	ds_read_b128 v[182:185], v194 offset:0x2000
	s_waitcnt lgkmcnt(4)
	v_mfma_f32_16x16x32_f16 v[218:221], v[98:101], v[158:161], 0
	ds_read_b128 v[222:225], v194 offset:0x3000
	s_waitcnt lgkmcnt(4)
	v_mfma_f32_16x16x32_f16 v[226:229], v[98:101], v[162:165], 0
	ds_read_b128 v[150:153], v195 offset:0
	s_waitcnt lgkmcnt(4)
	v_mfma_f32_16x16x32_f16 v[166:169], v[110:113], v[166:169], v[170:173]
	ds_read_b128 v[154:157], v195 offset:0x1000
	s_waitcnt lgkmcnt(4)
	v_mfma_f32_16x16x32_f16 v[170:173], v[110:113], v[174:177], v[178:181]
	ds_read_b128 v[158:161], v195 offset:0x2000
	s_waitcnt lgkmcnt(4)
	v_mfma_f32_16x16x32_f16 v[174:177], v[110:113], v[182:185], v[218:221]
	ds_read_b128 v[162:165], v195 offset:0x3000
	s_waitcnt lgkmcnt(4)
	s_and_b64 vcc, exec, vcc
	v_mfma_f32_16x16x32_f16 v[178:181], v[110:113], v[222:225], v[226:229]
	s_cbranch_vccnz .LBB6_16
	v_exp_f32_e32 v142, v142
	v_exp_f32_e32 v143, v143
	v_exp_f32_e32 v138, v138
	v_exp_f32_e32 v139, v139
	v_add_f32_e32 v142, 1.0, v142
	v_rcp_f32_e32 v142, v142
	v_add_f32_e32 v143, 1.0, v143
	v_rcp_f32_e32 v143, v143
	v_add_f32_e32 v138, 1.0, v138
	v_fmac_f32_e32 v134, v146, v142
	v_exp_f32_e32 v142, v134
	v_fmac_f32_e32 v135, v147, v143
	v_exp_f32_e32 v143, v135
	v_rcp_f32_e32 v134, v138
	v_add_f32_e32 v135, 1.0, v142
	v_rcp_f32_e32 v138, v135
	v_add_f32_e32 v135, 1.0, v139
	v_add_f32_e32 v139, 1.0, v143
	v_rcp_f32_e32 v139, v139
	v_cvt_f32_f16_sdwa v143, v0 dst_sel:DWORD dst_unused:UNUSED_PAD src0_sel:WORD_1
	v_cvt_f32_f16_e32 v142, v0
	v_exp_f32_e32 v0, v144
	v_rcp_f32_e32 v135, v135
	v_pk_fma_f32 v[138:139], v[138:139], 2.0, 1.0 op_sel_hi:[1,0,0] neg_lo:[1,0,0] neg_hi:[1,0,0]
	v_exp_f32_e32 v140, v140
	v_add_f32_e32 v0, 1.0, v0
	v_pk_fma_f32 v[138:139], v[134:135], v[138:139], v[138:139] neg_lo:[1,0,0] neg_hi:[1,0,0]
	v_rcp_f32_e32 v0, v0
	v_pk_fma_f32 v[134:135], v[134:135], v[142:143], v[138:139]
	v_exp_f32_e32 v138, v145
	v_add_f32_e32 v139, 1.0, v140
	v_fmac_f32_e32 v136, v148, v0
	v_exp_f32_e32 v0, v136
	v_add_f32_e32 v136, 1.0, v138
	v_rcp_f32_e32 v138, v136
	v_rcp_f32_e32 v136, v139
	v_exp_f32_e32 v139, v141
	v_add_f32_e32 v0, 1.0, v0
	v_fmac_f32_e32 v137, v149, v138
	v_exp_f32_e32 v140, v137
	v_rcp_f32_e32 v138, v0
	v_add_f32_e32 v0, 1.0, v139
	v_rcp_f32_e32 v137, v0
	v_add_f32_e32 v0, 1.0, v140
	v_rcp_f32_e32 v139, v0
	v_cvt_f32_f16_sdwa v141, v1 dst_sel:DWORD dst_unused:UNUSED_PAD src0_sel:WORD_1
	v_cvt_f32_f16_e32 v140, v1
	v_cvt_pk_f16_f32 v0, v134, v135
	v_pk_fma_f32 v[134:135], v[138:139], 2.0, 1.0 op_sel_hi:[1,0,0] neg_lo:[1,0,0] neg_hi:[1,0,0]
	s_nop 0
	v_pk_fma_f32 v[134:135], v[136:137], v[134:135], v[134:135] neg_lo:[1,0,0] neg_hi:[1,0,0]
	s_nop 0
	v_pk_fma_f32 v[134:135], v[136:137], v[140:141], v[134:135]
	s_nop 0
	v_cvt_pk_f16_f32 v1, v134, v135
	v_add_u32_e32 v134, v193, v214
	global_store_dwordx2 v134, v[0:1], s[0:1] nt
.LBB6_16:
	v_or_b32_e32 v0, s23, v201
	v_cndmask_b32_e64 v0, v217, v0, s[4:5]
	ds_read_b128 v[134:137], v196 offset:0
	s_waitcnt lgkmcnt(4)
	v_mfma_f32_16x16x32_f16 v[138:141], v[114:117], v[150:153], v[166:169]
	ds_read_b128 v[142:145], v196 offset:0x1000
	s_waitcnt lgkmcnt(4)
	v_mfma_f32_16x16x32_f16 v[146:149], v[114:117], v[154:157], v[170:173]
	ds_read_b128 v[150:153], v196 offset:0x2000
	s_waitcnt lgkmcnt(4)
	v_mfma_f32_16x16x32_f16 v[154:157], v[114:117], v[158:161], v[174:177]
	ds_read_b128 v[158:161], v196 offset:0x3000
	s_waitcnt lgkmcnt(4)
	v_mfma_f32_16x16x32_f16 v[162:165], v[114:117], v[162:165], v[178:181]
	ds_read_b128 v[166:169], v0 offset:0
	s_waitcnt lgkmcnt(4)
	v_mfma_f32_16x16x32_f16 v[134:137], v[106:109], v[134:137], v[138:141]
	ds_read_b128 v[138:141], v0 offset:0x100
	s_waitcnt lgkmcnt(4)
	v_mfma_f32_16x16x32_f16 v[142:145], v[106:109], v[142:145], v[146:149]
	ds_read_b128 v[146:149], v0 offset:0x200
	s_waitcnt lgkmcnt(4)
	v_mfma_f32_16x16x32_f16 v[150:153], v[106:109], v[150:153], v[154:157]
	ds_read_b128 v[154:157], v0 offset:0x300
	s_waitcnt lgkmcnt(4)
	v_mfma_f32_16x16x32_f16 v[158:161], v[106:109], v[158:161], v[162:165]
	s_waitcnt lgkmcnt(3)
	v_mfma_f32_16x16x32_f16 v[134:137], v[102:105], v[166:169], v[134:137]
	s_waitcnt lgkmcnt(2)
	v_mfma_f32_16x16x32_f16 v[138:141], v[102:105], v[138:141], v[142:145]
	s_waitcnt lgkmcnt(1)
	v_mfma_f32_16x16x32_f16 v[142:145], v[102:105], v[146:149], v[150:153]
	s_waitcnt lgkmcnt(0)
	v_mfma_f32_16x16x32_f16 v[146:149], v[102:105], v[154:157], v[158:161]
	s_nop 1
	v_cvt_pk_f16_f32 v1, v136, v137
	v_pk_max_f16 v1, v1, 0
	v_cvt_pk_f16_f32 v0, v134, v135
	v_pk_max_f16 v0, v0, 0
	v_cvt_pk_f16_f32 v135, v140, v141
	v_pk_max_f16 v135, v135, 0
	v_cvt_pk_f16_f32 v134, v138, v139
	v_pk_max_f16 v134, v134, 0
	ds_write2st64_b64 v216, v[0:1], v[134:135] offset1:8
	v_cvt_pk_f16_f32 v1, v144, v145
	v_pk_max_f16 v1, v1, 0
	v_cvt_pk_f16_f32 v0, v142, v143
	v_pk_max_f16 v0, v0, 0
	v_cvt_pk_f16_f32 v135, v148, v149
	v_pk_max_f16 v135, v135, 0
	v_cvt_pk_f16_f32 v134, v146, v147
	v_pk_max_f16 v134, v134, 0
	ds_write2st64_b64 v216, v[0:1], v[134:135] offset0:16 offset1:24
	s_waitcnt lgkmcnt(0)
	s_barrier
	ds_read_b128 v[134:137], v197 offset:0
	ds_read_b128 v[138:141], v198 offset:0
	ds_read_b128 v[142:145], v199 offset:0
	ds_read_b128 v[146:149], v200 offset:0
	ds_read_b128 v[150:153], v206 offset:0
	v_add_u32_e32 v0, s16, v213
	s_waitcnt lgkmcnt(4)
	v_min_i32_e32 v0, s11, v0
	v_mfma_f32_16x16x32_f16 v[154:157], v[2:5], v[134:137], v[118:121]
	v_cndmask_b32_e64 v0, v190, v0, s[8:9]
	v_ashrrev_i32_e32 v1, 31, v0
	ds_read_b128 v[162:165], v207 offset:0
	v_mfma_f32_16x16x32_f16 v[158:161], v[42:45], v[134:137], v[122:125]
	s_waitcnt lgkmcnt(4)
	v_lshlrev_b64 v[0:1], 5, v[0:1]
	v_lshl_add_u64 v[0:1], s[14:15], 0, v[0:1]
	v_mfma_f32_16x16x32_f16 v[134:137], v[66:69], v[134:137], v[126:129]
	v_lshl_add_u64 v[170:171], v[0:1], 0, 16
	v_mfma_f32_16x16x32_f16 v[154:157], v[6:9], v[138:141], v[154:157]
	v_mfma_f32_16x16x32_f16 v[158:161], v[46:49], v[138:141], v[158:161]
	v_mfma_f32_16x16x32_f16 v[166:169], v[70:73], v[138:141], v[134:137]
	s_cmp_lg_u32 s24, 0
	s_cbranch_scc1 .Lfirst_norows
	global_load_dwordx4 v[138:141], v[0:1], off
	global_load_dwordx4 v[134:137], v[170:171], off

.Lfirst_nogidx:
	v_mfma_f32_16x16x32_f16 v[142:145], v[74:77], v[142:145], v[166:169]
	ds_read_b128 v[166:169], v209 offset:0
	s_waitcnt lgkmcnt(4)
	v_mfma_f32_16x16x32_f16 v[154:157], v[10:13], v[146:149], v[154:157]
	v_mfma_f32_16x16x32_f16 v[158:161], v[58:61], v[146:149], v[158:161]
	v_mfma_f32_16x16x32_f16 v[146:149], v[90:93], v[146:149], v[142:145]
	ds_read_b128 v[142:145], v197 offset:0x1000
	s_waitcnt lgkmcnt(4)
	ds_read_b128 v[174:177], v198 offset:0x1000
	s_waitcnt lgkmcnt(4)
	v_mfma_f32_16x16x32_f16 v[154:157], v[14:17], v[150:153], v[154:157]
	v_mfma_f32_16x16x32_f16 v[158:161], v[22:25], v[150:153], v[158:161]
	v_mfma_f32_16x16x32_f16 v[150:153], v[86:89], v[150:153], v[130:133]
	v_mfma_f32_16x16x32_f16 v[154:157], v[26:29], v[162:165], v[154:157]
	v_mfma_f32_16x16x32_f16 v[158:161], v[34:37], v[162:165], v[158:161]
	v_mfma_f32_16x16x32_f16 v[150:153], v[78:81], v[162:165], v[150:153]
	ds_read_b128 v[162:165], v199 offset:0x1000
	s_waitcnt lgkmcnt(4)
	v_mfma_f32_16x16x32_f16 v[154:157], v[30:33], v[170:173], v[154:157]
	v_mfma_f32_16x16x32_f16 v[158:161], v[38:41], v[170:173], v[158:161]
	v_mfma_f32_16x16x32_f16 v[150:153], v[82:85], v[170:173], v[150:153]
	ds_read_b128 v[170:173], v200 offset:0x1000
	s_waitcnt lgkmcnt(4)
	v_mfma_f32_16x16x32_f16 v[154:157], v[54:57], v[166:169], v[154:157]
	v_mfma_f32_16x16x32_f16 v[158:161], v[62:65], v[166:169], v[158:161]
	v_mfma_f32_16x16x32_f16 v[150:153], v[94:97], v[166:169], v[150:153]
	s_nop 5
	v_exp_f32_e32 v154, v154
	v_exp_f32_e32 v158, v158
	ds_read_b64 v[0:1], v204 offset:0
	ds_read_b128 v[166:169], v206 offset:0x1000
	v_add_f32_e32 v154, 1.0, v154
	v_rcp_f32_e32 v154, v154
	v_add_f32_e32 v158, 1.0, v158
	s_waitcnt lgkmcnt(5)
	ds_read_b128 v[220:223], v207 offset:0x1000
	v_fma_f32 v146, v154, v150, v146
	v_exp_f32_e32 v146, v146
	v_exp_f32_e32 v154, v155
	v_rcp_f32_e32 v150, v158
	v_mfma_f32_16x16x32_f16 v[178:181], v[2:5], v[142:145], v[118:121]
	v_add_f32_e32 v146, 1.0, v146
	v_add_f32_e32 v154, 1.0, v154
	v_rcp_f32_e32 v146, v146
	v_rcp_f32_e32 v154, v154
	v_mfma_f32_16x16x32_f16 v[182:185], v[42:45], v[142:145], v[122:125]
	s_waitcnt lgkmcnt(5)
	v_fma_f32 v146, v146, -2.0, 1.0
	v_fma_f32 v147, v154, v151, v147
	v_mfma_f32_16x16x32_f16 v[142:145], v[66:69], v[142:145], v[126:129]
	v_fma_f32 v146, -v150, v146, v146
	v_exp_f32_e32 v147, v147
	s_waitcnt lgkmcnt(2)
	v_mfma_f32_16x16x32_f16 v[178:181], v[6:9], v[174:177], v[178:181]
	v_fma_mixlo_f16 v146, v150, v0, v146 op_sel_hi:[0,1,0]
	v_exp_f32_e32 v150, v159
	v_add_f32_e32 v147, 1.0, v147
	v_mfma_f32_16x16x32_f16 v[182:185], v[46:49], v[174:177], v[182:185]
	v_rcp_f32_e32 v151, v147
	v_add_f32_e32 v150, 1.0, v150
	v_rcp_f32_e32 v150, v150
	v_mfma_f32_16x16x32_f16 v[142:145], v[70:73], v[174:177], v[142:145]
	ds_read_b128 v[174:177], v208 offset:0x1000
	s_waitcnt lgkmcnt(5)
	v_cmp_eq_u32_e32 vcc, s16, v211
	v_mfma_f32_16x16x32_f16 v[178:181], v[50:53], v[162:165], v[178:181]
	v_add_u32_e32 v218, v193, v210
	v_cndmask_b32_e64 v189, v146, 0, vcc
	v_add_u32_e32 v188, 0x1000, v218
	v_mfma_f32_16x16x32_f16 v[182:185], v[18:21], v[162:165], v[182:185]
	v_mfma_f32_16x16x32_f16 v[142:145], v[74:77], v[162:165], v[142:145]
	ds_read_b128 v[162:165], v209 offset:0x1000
	s_waitcnt lgkmcnt(5)
	v_mfma_f32_16x16x32_f16 v[178:181], v[10:13], v[170:173], v[178:181]
	v_mfma_f32_16x16x32_f16 v[182:185], v[58:61], v[170:173], v[182:185]
	v_mfma_f32_16x16x32_f16 v[144:147], v[90:93], v[170:173], v[142:145]
	s_nop 3
	v_fma_f32 v142, v151, -2.0, 1.0
	v_fma_f32 v142, -v150, v142, v142
	v_fma_mixlo_f16 v0, v150, v0, v142 op_sel:[0,1,0] op_sel_hi:[0,1,0]
	v_cndmask_b32_e64 v0, v0, 0, vcc
	v_exp_f32_e32 v142, v156
	ds_read_b128 v[170:173], v197 offset:0x2000
	s_waitcnt lgkmcnt(4)
	v_exp_f32_e32 v143, v160
	v_add_f32_e32 v142, 1.0, v142
	v_rcp_f32_e32 v142, v142
	v_mfma_f32_16x16x32_f16 v[182:185], v[22:25], v[166:169], v[182:185]
	ds_read_b128 v[224:227], v198 offset:0x2000
	s_waitcnt lgkmcnt(4)
	v_fma_f32 v142, v142, v152, v148
	v_exp_f32_e32 v148, v157
	v_mfma_f32_16x16x32_f16 v[178:181], v[14:17], v[166:169], v[178:181]
	v_exp_f32_e32 v142, v142
	v_add_f32_e32 v143, 1.0, v143
	v_add_f32_e32 v148, 1.0, v148
	v_rcp_f32_e32 v148, v148
	v_mfma_f32_16x16x32_f16 v[166:169], v[86:89], v[166:169], v[130:133]
	v_add_f32_e32 v142, 1.0, v142
	v_rcp_f32_e32 v142, v142
	v_rcp_f32_e32 v143, v143
	v_mfma_f32_16x16x32_f16 v[182:185], v[34:37], v[220:223], v[182:185]
	v_fmac_f32_e32 v149, v148, v153
	v_exp_f32_e32 v150, v161
	v_fma_f32 v142, v142, -2.0, 1.0
	v_mfma_f32_16x16x32_f16 v[178:181], v[26:29], v[220:223], v[178:181]
	v_fma_f32 v142, -v143, v142, v142
	v_fma_mixlo_f16 v142, v143, v1, v142 op_sel_hi:[0,1,0]
	v_add_f32_e32 v143, 1.0, v150
	v_mfma_f32_16x16x32_f16 v[154:157], v[78:81], v[220:223], v[166:169]
	ds_read_b128 v[166:169], v199 offset:0x2000
	s_waitcnt lgkmcnt(4)
	v_rcp_f32_e32 v143, v143
	v_mfma_f32_16x16x32_f16 v[158:161], v[38:41], v[174:177], v[182:185]
	v_cndmask_b32_e64 v142, v142, 0, vcc
	v_pack_b32_f16 v0, v189, v0
	s_nop 0
	v_exp_f32_e32 v182, v149
	v_mfma_f32_16x16x32_f16 v[178:181], v[30:33], v[174:177], v[178:181]
	v_mfma_f32_16x16x32_f16 v[148:151], v[82:85], v[174:177], v[154:157]
	ds_read_b128 v[152:155], v200 offset:0x2000
	s_waitcnt lgkmcnt(4)
	v_mfma_f32_16x16x32_f16 v[174:177], v[54:57], v[162:165], v[178:181]
	s_nop 0
	v_add_f32_e32 v156, 1.0, v182
	s_nop 2
	v_rcp_f32_e32 v178, v156
	v_mfma_f32_16x16x32_f16 v[156:159], v[62:65], v[162:165], v[158:161]
	s_nop 2
	v_fma_f32 v160, v178, -2.0, 1.0
	v_fma_f32 v160, -v143, v160, v160
	v_mfma_f32_16x16x32_f16 v[148:151], v[94:97], v[162:165], v[148:151]
	v_fma_mixlo_f16 v1, v143, v1, v160 op_sel:[0,1,0] op_sel_hi:[0,1,0]
	v_cndmask_b32_e64 v1, v1, 0, vcc
	v_pack_b32_f16 v1, v142, v1
	global_store_dwordx2 v188, v[0:1], s[0:1] nt
	v_exp_f32_e32 v142, v174
	v_exp_f32_e32 v143, v156
	ds_read_b64 v[0:1], v204 offset:0x1000
	ds_read_b128 v[160:163], v206 offset:0x2000
	v_add_f32_e32 v142, 1.0, v142
	v_rcp_f32_e32 v142, v142
	s_waitcnt lgkmcnt(5)
	v_add_f32_e32 v143, 1.0, v143
	v_mfma_f32_16x16x32_f16 v[178:181], v[2:5], v[170:173], v[118:121]
	v_fma_f32 v142, v142, v148, v144
	v_exp_f32_e32 v144, v175
	v_exp_f32_e32 v142, v142
	v_mfma_f32_16x16x32_f16 v[182:185], v[42:45], v[170:173], v[122:125]
	v_rcp_f32_e32 v143, v143
	v_add_f32_e32 v144, 1.0, v144
	v_add_f32_e32 v142, 1.0, v142
	v_mfma_f32_16x16x32_f16 v[170:173], v[66:69], v[170:173], v[126:129]
	v_rcp_f32_e32 v144, v144
	v_rcp_f32_e32 v142, v142
	ds_read_b128 v[220:223], v207 offset:0x2000
	s_waitcnt lgkmcnt(5)
	v_fma_f32 v148, v144, v149, v145
	v_mfma_f32_16x16x32_f16 v[178:181], v[6:9], v[224:227], v[178:181]
	v_fma_f32 v142, v142, -2.0, 1.0
	v_exp_f32_e32 v148, v148
	v_fma_f32 v142, -v143, v142, v142
	v_mfma_f32_16x16x32_f16 v[182:185], v[46:49], v[224:227], v[182:185]
	v_exp_f32_e32 v149, v157
	s_waitcnt lgkmcnt(2)
	v_add_f32_e32 v148, 1.0, v148
	v_mfma_f32_16x16x32_f16 v[170:173], v[70:73], v[224:227], v[170:173]
	ds_read_b128 v[224:227], v208 offset:0x2000
	s_waitcnt lgkmcnt(5)
	v_fma_mixlo_f16 v188, v143, v0, v142 op_sel_hi:[0,1,0]
	v_mfma_f32_16x16x32_f16 v[178:181], v[50:53], v[166:169], v[178:181]
	v_rcp_f32_e32 v148, v148
	v_add_f32_e32 v149, 1.0, v149
	v_rcp_f32_e32 v232, v149
	v_mfma_f32_16x16x32_f16 v[182:185], v[18:21], v[166:169], v[182:185]
	v_fma_f32 v148, v148, -2.0, 1.0
	v_add_u32_e32 v219, 0x2000, v218
	v_fma_f32 v233, -v232, v148, v148
	v_mfma_f32_16x16x32_f16 v[142:145], v[74:77], v[166:169], v[170:173]
	ds_read_b128 v[170:173], v209 offset:0x2000
	s_waitcnt lgkmcnt(5)
	v_mfma_f32_16x16x32_f16 v[164:167], v[10:13], v[152:155], v[178:181]
	v_mfma_f32_16x16x32_f16 v[178:181], v[58:61], v[152:155], v[182:185]
	v_mfma_f32_16x16x32_f16 v[142:145], v[90:93], v[152:155], v[142:145]
	v_exp_f32_e32 v148, v176
	v_exp_f32_e32 v149, v158
	ds_read_b128 v[228:231], v197 offset:0x3000
	s_waitcnt lgkmcnt(4)
	v_add_f32_e32 v148, 1.0, v148
	v_rcp_f32_e32 v148, v148
	v_mfma_f32_16x16x32_f16 v[152:155], v[14:17], v[160:163], v[164:167]
	v_fma_mixhi_f16 v188, v232, v0, v233 op_sel:[0,1,0] op_sel_hi:[0,1,0]
	v_fma_f32 v146, v148, v150, v146
	v_add_f32_e32 v148, 1.0, v149
	v_exp_f32_e32 v149, v177
	v_mfma_f32_16x16x32_f16 v[166:169], v[22:25], v[160:163], v[178:181]
	v_exp_f32_e32 v146, v146
	v_exp_f32_e32 v150, v159
	v_add_f32_e32 v149, 1.0, v149
	v_rcp_f32_e32 v149, v149
	v_mfma_f32_16x16x32_f16 v[178:181], v[86:89], v[160:163], v[130:133]
	ds_read_b128 v[162:165], v198 offset:0x3000
	s_waitcnt lgkmcnt(4)
	v_fmac_f32_e32 v147, v149, v151
	v_exp_f32_e32 v147, v147
	v_add_f32_e32 v146, 1.0, v146
	v_mfma_f32_16x16x32_f16 v[152:155], v[26:29], v[220:223], v[152:155]
	v_rcp_f32_e32 v146, v146
	v_add_f32_e32 v147, 1.0, v147
	v_rcp_f32_e32 v148, v148
	v_mfma_f32_16x16x32_f16 v[182:185], v[34:37], v[220:223], v[166:169]
	v_add_f32_e32 v150, 1.0, v150
	v_rcp_f32_e32 v147, v147
	v_rcp_f32_e32 v150, v150
	v_mfma_f32_16x16x32_f16 v[174:177], v[78:81], v[220:223], v[178:181]
	ds_read_b128 v[166:169], v199 offset:0x3000
	s_waitcnt lgkmcnt(4)
	v_fma_f32 v146, v146, -2.0, 1.0
	v_mfma_f32_16x16x32_f16 v[152:155], v[30:33], v[224:227], v[152:155]
	v_fma_f32 v146, -v148, v146, v146
	v_fma_f32 v151, v147, -2.0, 1.0
	v_fma_mixlo_f16 v189, v148, v1, v146 op_sel_hi:[0,1,0]
	v_mfma_f32_16x16x32_f16 v[178:181], v[38:41], v[224:227], v[182:185]
	v_fma_f32 v151, -v150, v151, v151
	ds_read_b128 v[158:161], v200 offset:0x3000
	s_waitcnt lgkmcnt(4)
	v_mfma_f32_16x16x32_f16 v[174:177], v[82:85], v[224:227], v[174:177]
	v_fma_mixhi_f16 v189, v150, v1, v151 op_sel:[0,1,0] op_sel_hi:[0,1,0]
	global_store_dwordx2 v219, v[188:189], s[0:1] nt
	v_mfma_f32_16x16x32_f16 v[154:157], v[54:57], v[170:173], v[152:155]
	v_mfma_f32_16x16x32_f16 v[146:149], v[62:65], v[170:173], v[178:181]
	v_mfma_f32_16x16x32_f16 v[150:153], v[94:97], v[170:173], v[174:177]
	ds_read_b64 v[188:189], v204 offset:0x2000
	ds_read_b64 v[0:1], v204 offset:0x3000
	ds_read_b128 v[170:173], v206 offset:0x3000
	s_waitcnt lgkmcnt(6)
	s_waitcnt vmcnt(2)
	v_mfma_f32_16x16x32_f16 v[182:185], v[2:5], v[228:231], v[118:121]
	v_mfma_f32_16x16x32_f16 v[174:177], v[42:45], v[228:231], v[122:125]
	v_mfma_f32_16x16x32_f16 v[178:181], v[66:69], v[228:231], v[126:129]
	s_and_saveexec_b64 s[2:3], s[6:7]
	s_cbranch_execz .LBB6_13
	s_xor_b32 s23, s23, 0x1000
	v_cvt_pk_f16_f32 v221, v140, v141
	v_cvt_pk_f16_f32 v220, v138, v139
	v_cvt_pk_f16_f32 v223, v136, v137
	v_cvt_pk_f16_f32 v222, v134, v135
	v_add_u32_e32 v134, s23, v205
	ds_write_b128 v134, v[220:223] offset:49152
	s_branch .LBB6_13

.Lnode_nofeat:
	v_subrev_u32_e32 v27, 52, v46
	v_min_u32_e32 v27, s16, v27
	global_load_dword v27, v27, s[8:9]
	global_load_dword v92, v56, s[8:9]
	v_subrev_u32_e32 v56, 48, v46
	v_min_u32_e32 v56, s17, v56
	global_load_dword v93, v56, s[8:9]
	v_min_u32_e32 v56, s17, v46
	global_load_dword v94, v56, s[8:9]
	v_subrev_u32_e32 v56, 56, v46
	v_min_u32_e32 v56, s15, v56
	global_load_dword v95, v56, s[8:9]
	v_add_u32_e32 v56, -8, v46
	s_add_i32 s25, s24, s19
	v_min_u32_e32 v56, s15, v56
	global_load_dword v96, v56, s[8:9]
	v_lshl_or_b32 v50, v50, 8, v29
	s_add_i32 m0, s25, 0x4000
	s_add_i32 s24, s24, s20
	global_load_lds_dwordx4 v50, s[4:5]
	v_lshl_or_b32 v50, v51, 8, v31
	s_add_i32 m0, s24, 0x4000
	s_add_i32 s2, s2, s3
	global_load_lds_dwordx4 v50, s[4:5]
	v_or_b32_e32 v50, s23, v32
	v_or_b32_e32 v51, s23, v33
	v_or_b32_e32 v97, s23, v34
	v_or_b32_e32 v98, s23, v35
	ds_read_b128 v[56:59], v50 offset:0
	ds_read_b128 v[60:63], v50 offset:0x1000
	ds_read_b128 v[64:67], v50 offset:0x2000
	ds_read_b128 v[68:71], v50 offset:0x3000
	ds_read_b128 v[72:75], v51 offset:0
	s_nop 0
	s_waitcnt lgkmcnt(4)
	v_mfma_f32_16x16x32_f16 v[56:59], v[14:17], v[56:59], 0
	ds_read_b128 v[76:79], v51 offset:0x1000
	s_waitcnt lgkmcnt(4)
	v_mfma_f32_16x16x32_f16 v[60:63], v[14:17], v[60:63], 0
	ds_read_b128 v[80:83], v51 offset:0x2000
	s_waitcnt lgkmcnt(4)
	v_mfma_f32_16x16x32_f16 v[64:67], v[14:17], v[64:67], 0
	ds_read_b128 v[84:87], v51 offset:0x3000
	s_waitcnt lgkmcnt(4)
	v_mfma_f32_16x16x32_f16 v[68:71], v[14:17], v[68:71], 0
	ds_read_b128 v[88:91], v97 offset:0
	s_waitcnt lgkmcnt(4)
	v_mfma_f32_16x16x32_f16 v[56:59], v[2:5], v[72:75], v[56:59]
	ds_read_b128 v[72:75], v97 offset:0x1000
	s_waitcnt lgkmcnt(4)
	v_mfma_f32_16x16x32_f16 v[60:63], v[2:5], v[76:79], v[60:63]
	ds_read_b128 v[76:79], v97 offset:0x2000
	s_waitcnt lgkmcnt(4)
	v_mfma_f32_16x16x32_f16 v[64:67], v[2:5], v[80:83], v[64:67]
	ds_read_b128 v[80:83], v97 offset:0x3000
	s_waitcnt lgkmcnt(4)
	v_mfma_f32_16x16x32_f16 v[68:71], v[2:5], v[84:87], v[68:71]
	ds_read_b128 v[84:87], v98 offset:0
	s_waitcnt lgkmcnt(4)
	v_mfma_f32_16x16x32_f16 v[56:59], v[6:9], v[88:91], v[56:59]
	ds_read_b128 v[88:91], v98 offset:0x1000
	s_waitcnt lgkmcnt(4)
	v_mfma_f32_16x16x32_f16 v[60:63], v[6:9], v[72:75], v[60:63]
	ds_read_b128 v[72:75], v98 offset:0x2000
	s_waitcnt lgkmcnt(4)
	v_mfma_f32_16x16x32_f16 v[64:67], v[6:9], v[76:79], v[64:67]
	ds_read_b128 v[76:79], v98 offset:0x3000
	s_waitcnt lgkmcnt(4)
	v_mfma_f32_16x16x32_f16 v[68:71], v[6:9], v[80:83], v[68:71]
	ds_read_b128 v[80:83], v37 offset:0
	s_waitcnt lgkmcnt(4)
	v_mfma_f32_16x16x32_f16 v[56:59], v[10:13], v[84:87], v[56:59]
	ds_read_b128 v[84:87], v37 offset:0x100
	s_waitcnt lgkmcnt(4)
	v_mfma_f32_16x16x32_f16 v[60:63], v[10:13], v[88:91], v[60:63]
	ds_read_b128 v[88:91], v37 offset:0x200
	s_waitcnt lgkmcnt(4)
	v_mfma_f32_16x16x32_f16 v[64:67], v[10:13], v[72:75], v[64:67]
	ds_read_b128 v[72:75], v37 offset:0x300
	s_waitcnt lgkmcnt(4)
	v_mfma_f32_16x16x32_f16 v[68:71], v[10:13], v[76:79], v[68:71]
	s_waitcnt lgkmcnt(3)
	v_mfma_f32_16x16x32_f16 v[56:59], v[18:21], v[80:83], v[56:59]
	s_waitcnt lgkmcnt(2)
	v_mfma_f32_16x16x32_f16 v[60:63], v[18:21], v[84:87], v[60:63]
	s_waitcnt lgkmcnt(1)
	v_mfma_f32_16x16x32_f16 v[64:67], v[18:21], v[88:91], v[64:67]
	s_waitcnt lgkmcnt(0)
	v_mfma_f32_16x16x32_f16 v[68:71], v[18:21], v[72:75], v[68:71]
	s_nop 1
	v_cvt_pk_f16_f32 v51, v58, v59
	v_pk_max_f16 v51, v51, 0
	v_cvt_pk_f16_f32 v50, v56, v57
	v_pk_max_f16 v50, v50, 0
	v_cvt_pk_f16_f32 v57, v62, v63
	v_pk_max_f16 v57, v57, 0
	v_cvt_pk_f16_f32 v56, v60, v61
	v_pk_max_f16 v56, v56, 0
	ds_write2st64_b64 v48, v[50:51], v[56:57] offset1:8
	v_cvt_pk_f16_f32 v51, v66, v67
	v_pk_max_f16 v51, v51, 0
	v_cvt_pk_f16_f32 v50, v64, v65
	v_pk_max_f16 v50, v50, 0
	v_cvt_pk_f16_f32 v57, v70, v71
	v_pk_max_f16 v57, v57, 0
	v_cvt_pk_f16_f32 v56, v68, v69
	v_pk_max_f16 v56, v56, 0
	ds_write2st64_b64 v48, v[50:51], v[56:57] offset0:16 offset1:24
	s_waitcnt lgkmcnt(0)
	s_barrier
	v_lshl_or_b32 v40, v40, 8, v29
	s_add_i32 m0, s25, 0x8000
	s_xor_b64 s[6:7], s[6:7], -1
	global_load_lds_dwordx4 v40, s[4:5]
	v_lshl_or_b32 v40, v41, 8, v31
	s_add_i32 m0, s24, 0x8000
	v_add_u32_e32 v46, s22, v46
	global_load_lds_dwordx4 v40, s[4:5]
	v_lshl_or_b32 v40, v42, 8, v29
	s_mov_b32 m0, s25
	s_nop 0
	global_load_lds_dwordx4 v40, s[4:5]
	v_lshl_or_b32 v40, v45, 8, v31
	s_mov_b32 m0, s24
	s_nop 0
	global_load_lds_dwordx4 v40, s[4:5]
	v_add_u32_e32 v40, v39, v43
	ds_read_b128 v[56:59], v40
	ds_read_b128 v[60:63], v49
	v_add_u32_e32 v40, s18, v38
	v_ashrrev_i32_e32 v41, 31, v40
	v_lshlrev_b64 v[50:51], 8, v[40:41]
	v_add_u32_e32 v40, 32, v40
	v_ashrrev_i32_e32 v41, 31, v40
	v_lshlrev_b64 v[40:41], 8, v[40:41]
	v_lshl_add_u64 v[50:51], v[0:1], 0, v[50:51]
	v_lshl_add_u64 v[40:41], v[0:1], 0, v[40:41]
	s_waitcnt lgkmcnt(0)
	global_store_dwordx4 v[50:51], v[56:59], off
	global_store_dwordx4 v[40:41], v[60:63], off
	s_add_i32 s18, s18, s21
	s_waitcnt vmcnt(8)
	s_cmp_lt_i32 s2, s13
	v_mov_b32_e32 v50, v27
	v_mov_b32_e32 v51, v92
	v_mov_b32_e32 v40, v93
	v_mov_b32_e32 v41, v94
	v_mov_b32_e32 v42, v95
	v_mov_b32_e32 v45, v96
	s_cbranch_scc0 .LBB8_8
